# P3 loop1: second 12-load batch hoisted behind first into free VGPRs (MLP), on top of combo1
# speedup vs baseline: 1.0086x; 1.0014x over previous
; #define GAS __attribute__((address_space(1)))
; __device__ __forceinline__ void unpack8(const u32x4 v, float (&f)[8]) { f[0] = bflo(v.x); f[1] = bfhi(v.x); f[2] = bflo(v.y); f[3] = bfhi(v.y); f[4] = bflo(v.z); f[5] = bfhi(v.z); f[6] = bflo(v.w); f[7] = bfhi(v.w); }
; __device__ __forceinline__ void p3_rows2(int row0, const bf16* PROJ, const float* sc_w, const float* sc_nw, const float* ssd_nw, const float* SSQ, bf16* Y, LAS unsigned char* scr, int lane) {
;     ...
;     for (int i = 0; i < 8; ++i) {
;         const int c0 = (i * 64 + lane) * 8; const bf16* q = pr + i * 512; const bf16* qh = halo ? q : q + 2 * PP;
;         const u32x4 um2v = *(const GAS u32x4*)(qh - 2 * PP + O_U), um1v = *(const GAS u32x4*)(qh - PP + O_U), u0v = *(const GAS u32x4*)(q + O_U), u1v = *(const GAS u32x4*)(q + PP + O_U);
;         const u32x4 b0v = *(const GAS u32x4*)(q + O_SCB), b1v = *(const GAS u32x4*)(q + PP + O_SCB);
;         const f32x4 w0a = *(const GAS f32x4*)(sc_w + c0), w0b = *(const GAS f32x4*)(sc_w + c0 + 4), w1a = *(const GAS f32x4*)(sc_w + D_CONV + c0), w1b = *(const GAS f32x4*)(sc_w + D_CONV + c0 + 4),
;                     w2a = *(const GAS f32x4*)(sc_w + 2 * D_CONV + c0), w2b = *(const GAS f32x4*)(sc_w + 2 * D_CONV + c0 + 4);
;         const float w0[8] = {w0a.x, w0a.y, w0a.z, w0a.w, w0b.x, w0b.y, w0b.z, w0b.w}, w1[8] = {w1a.x, w1a.y, w1a.z, w1a.w, w1b.x, w1b.y, w1b.z, w1b.w}, w2[8] = {w2a.x, w2a.y, w2a.z, w2a.w, w2b.x, w2b.y, w2b.z, w2b.w};
;         float um2[8], um1[8], u0[8], u1[8], b0[8], b1[8];
;         unpack8(um2v, um2); unpack8(um1v, um1); unpack8(u0v, u0); unpack8(u1v, u1);
; #pragma unroll
;         for (int j = 0; j < 8; ++j) { um2[j] = halo ? um2[j] : 0.f; um1[j] = halo ? um1[j] : 0.f; }
;         unpack8(b0v, b0); unpack8(b1v, b1);
;         float y0[8], y1[8];
; #pragma unroll
;         for (int j = 0; j < 8; ++j) { y0[j] = b0[j] * (w2[j] * u0[j] + w0[j] * um2[j] + w1[j] * um1[j]); y1[j] = b1[j] * (w2[j] * u1[j] + w0[j] * um1[j] + w1[j] * u0[j]); ss0 += y0[j] * y0[j]; ss1 += y1[j] * y1[j]; }
.LBB0_485:
	v_lshl_add_u64 v[26:27], v[6:7], 0, s[2:3]
	s_waitcnt vmcnt(0)
	v_add_co_u32_e32 v76, vcc, 0xfffe3000, v26
	v_lshl_add_u64 v[24:25], v[14:15], 0, s[4:5]
	s_nop 0
	v_addc_co_u32_e32 v77, vcc, -1, v27, vcc
	v_add_co_u32_e32 v26, vcc, 0xfffec000, v26
	global_load_dwordx4 v[2:5], v[6:7], off offset:-1024
	s_nop 0
	v_addc_co_u32_e32 v27, vcc, -1, v27, vcc
	v_add_co_u32_e32 v82, vcc, 0xffff5000, v6
	global_load_dwordx4 v[32:35], v[24:25], off offset:16
	global_load_dwordx4 v[36:39], v[24:25], off
	v_addc_co_u32_e32 v83, vcc, -1, v7, vcc
	v_add_co_u32_e32 v84, vcc, 0xffffe000, v6
	global_load_dwordx4 v[40:43], v[76:77], off offset:-2560
	global_load_dwordx4 v[44:47], v[26:27], off offset:-2048
	v_addc_co_u32_e32 v85, vcc, -1, v7, vcc
	v_add_co_u32_e32 v86, vcc, 0xffff7000, v6
	v_lshl_add_u64 v[64:65], v[24:25], 0, s[18:19]
	s_nop 0
	v_addc_co_u32_e32 v87, vcc, -1, v7, vcc
	v_add_co_u32_e32 v88, vcc, s34, v24
	v_lshl_add_u64 v[72:73], v[24:25], 0, s[20:21]
	s_nop 0
	v_addc_co_u32_e32 v89, vcc, 0, v25, vcc
	v_add_co_u32_e32 v90, vcc, s35, v24
	global_load_dwordx4 v[48:51], v[82:83], off offset:-1536
	global_load_dwordx4 v[52:55], v[84:85], off offset:-1024
	v_addc_co_u32_e32 v91, vcc, 0, v25, vcc
	global_load_dwordx4 v[56:59], v[86:87], off offset:-1536
	global_load_dwordx4 v[60:63], v[88:89], off
	s_nop 0
	global_load_dwordx4 v[64:67], v[64:65], off offset:16
	s_nop 0
	global_load_dwordx4 v[68:71], v[90:91], off
	s_nop 0
	global_load_dwordx4 v[72:75], v[72:73], off offset:16
	v_lshl_add_u64 v[78:79], v[24:25], 0, s[22:23]
	v_lshl_add_u64 v[80:81], v[24:25], 0, s[24:25]
	global_load_dwordx4 v[184:187], v[76:77], off offset:-1536
	global_load_dwordx4 v[188:191], v[26:27], off offset:-1024
	global_load_dwordx4 v[192:195], v[82:83], off offset:-512
	global_load_dwordx4 v[196:199], v[84:85], off
	global_load_dwordx4 v[200:203], v[86:87], off offset:-512
	global_load_dwordx4 v[204:207], v[6:7], off
	global_load_dwordx4 v[208:211], v[90:91], off offset:2048
	global_load_dwordx4 v[212:215], v[24:25], off offset:2048
	global_load_dwordx4 v[216:219], v[88:89], off offset:2048
	global_load_dwordx4 v[220:223], v[80:81], off offset:16
	global_load_dwordx4 v[140:143], v[24:25], off offset:2064
	global_load_dwordx4 v[224:227], v[78:79], off offset:16
	s_add_u32 s4, s4, 0x1000
	s_addc_u32 s5, s5, 0
	s_cmpk_eq_i32 s4, 0x4000
	s_waitcnt vmcnt(23)
	v_lshlrev_b32_e32 v93, 16, v2
	v_and_b32_e32 v95, 0xffff0000, v2
	v_lshlrev_b32_e32 v99, 16, v4
	v_and_b32_e32 v101, 0xffff0000, v4
	s_waitcnt vmcnt(22)
	v_mov_b32_e32 v106, v35
	s_waitcnt vmcnt(21)
	v_mov_b32_e32 v104, v39
	v_lshlrev_b32_e32 v97, 16, v3
	v_and_b32_e32 v3, 0xffff0000, v3
	v_lshlrev_b32_e32 v103, 16, v5
	v_and_b32_e32 v5, 0xffff0000, v5
	s_waitcnt vmcnt(20)
	v_and_b32_e32 v2, 0xffff0000, v40
	v_lshlrev_b32_e32 v4, 16, v41
	v_lshlrev_b32_e32 v94, 16, v40
	s_waitcnt vmcnt(19)
	v_and_b32_e32 v100, 0xffff0000, v44
	v_lshlrev_b32_e32 v92, 16, v42
	v_and_b32_e32 v41, 0xffff0000, v41
	v_and_b32_e32 v96, 0xffff0000, v42
	v_lshlrev_b32_e32 v98, 16, v43
	v_and_b32_e32 v43, 0xffff0000, v43
	v_lshlrev_b32_e32 v102, 16, v45
	v_cndmask_b32_e64 v2, v2, 0, s[0:1]
	v_cndmask_b32_e64 v40, v4, 0, s[0:1]
	v_lshlrev_b32_e32 v4, 16, v44
	v_cndmask_b32_e64 v42, v94, 0, s[0:1]
	v_and_b32_e32 v94, 0xffff0000, v46
	v_cndmask_b32_e64 v118, v100, 0, s[0:1]
	v_lshlrev_b32_e32 v105, 16, v46
	v_cndmask_b32_e64 v44, v41, 0, s[0:1]
	v_cndmask_b32_e64 v108, v96, 0, s[0:1]
	v_cndmask_b32_e64 v112, v43, 0, s[0:1]
	s_waitcnt vmcnt(18)
	v_and_b32_e32 v114, 0xffff0000, v49
	v_lshlrev_b32_e32 v116, 16, v49
	v_cndmask_b32_e64 v41, v102, 0, s[0:1]
	v_lshlrev_b32_e32 v120, 16, v48
	v_cndmask_b32_e64 v43, v4, 0, s[0:1]
	v_mul_f32_e32 v122, v2, v37
	v_and_b32_e32 v48, 0xffff0000, v48
	v_lshlrev_b32_e32 v124, 16, v50
	v_and_b32_e32 v50, 0xffff0000, v50
	v_lshlrev_b32_e32 v126, 16, v51
	v_and_b32_e32 v128, 0xffff0000, v51
	v_cndmask_b32_e64 v109, v94, 0, s[0:1]
	s_waitcnt vmcnt(17)
	v_lshlrev_b32_e32 v117, 16, v53
	v_lshlrev_b32_e32 v121, 16, v52
	v_and_b32_e32 v49, 0xffff0000, v52
	v_mul_f32_e32 v123, v118, v37
	v_lshlrev_b32_e32 v125, 16, v54
	v_and_b32_e32 v51, 0xffff0000, v54
	v_lshlrev_b32_e32 v127, 16, v55
	v_and_b32_e32 v45, 0xffff0000, v45
	v_lshlrev_b32_e32 v107, 16, v47
	v_and_b32_e32 v113, 0xffff0000, v47
	v_cndmask_b32_e64 v46, v92, 0, s[0:1]
	v_cndmask_b32_e64 v47, v105, 0, s[0:1]
	v_and_b32_e32 v115, 0xffff0000, v53
	v_and_b32_e32 v129, 0xffff0000, v55
	v_mov_b32_e32 v119, v48
	v_pk_mov_b32 v[52:53], v[42:43], v[120:121] op_sel:[1,0]
	v_pk_mov_b32 v[54:55], v[40:41], v[116:117] op_sel:[1,0]
	v_pk_mov_b32 v[130:131], v[108:109], v[50:51] op_sel:[1,0]
	s_waitcnt vmcnt(13)
	v_pk_mul_f32 v[120:121], v[68:69], v[120:121] op_sel_hi:[0,1]
	v_pk_fma_f32 v[48:49], v[68:69], v[48:49], v[122:123] op_sel:[1,0,0]
	v_pk_mul_f32 v[68:69], v[70:71], v[116:117] op_sel_hi:[0,1]
	v_mov_b32_e32 v70, v71
	s_waitcnt vmcnt(12)
; #define GAS __attribute__((address_space(1)))
; #define LAS __attribute__((address_space(3)))
; __device__ __forceinline__ void unpack8(const u32x4 v, float (&f)[8]) { f[0] = bflo(v.x); f[1] = bfhi(v.x); f[2] = bflo(v.y); f[3] = bfhi(v.y); f[4] = bflo(v.z); f[5] = bfhi(v.z); f[6] = bflo(v.w); f[7] = bfhi(v.w); }
; __device__ __forceinline__ u32x4 pack8(const float (&f)[8]) { u32x4 o; o.x = cvtpk(f[0], f[1]); o.y = cvtpk(f[2], f[3]); o.z = cvtpk(f[4], f[5]); o.w = cvtpk(f[6], f[7]); return o; }
; __device__ __forceinline__ void p3_rows2(int row0, const bf16* PROJ, const float* sc_w, const float* sc_nw, const float* ssd_nw, const float* SSQ, bf16* Y, LAS unsigned char* scr, int lane) {
;     ...
;         const int c0 = (i * 64 + lane) * 8; const bf16* q = pr + i * 512; const bf16* qh = halo ? q : q + 2 * PP;
;         const u32x4 um2v = *(const GAS u32x4*)(qh - 2 * PP + O_U), um1v = *(const GAS u32x4*)(qh - PP + O_U), u0v = *(const GAS u32x4*)(q + O_U), u1v = *(const GAS u32x4*)(q + PP + O_U);
;         const u32x4 b0v = *(const GAS u32x4*)(q + O_SCB), b1v = *(const GAS u32x4*)(q + PP + O_SCB);
;         const f32x4 w0a = *(const GAS f32x4*)(sc_w + c0), w0b = *(const GAS f32x4*)(sc_w + c0 + 4), w1a = *(const GAS f32x4*)(sc_w + D_CONV + c0), w1b = *(const GAS f32x4*)(sc_w + D_CONV + c0 + 4),
;                     w2a = *(const GAS f32x4*)(sc_w + 2 * D_CONV + c0), w2b = *(const GAS f32x4*)(sc_w + 2 * D_CONV + c0 + 4);
;         const float w0[8] = {w0a.x, w0a.y, w0a.z, w0a.w, w0b.x, w0b.y, w0b.z, w0b.w}, w1[8] = {w1a.x, w1a.y, w1a.z, w1a.w, w1b.x, w1b.y, w1b.z, w1b.w}, w2[8] = {w2a.x, w2a.y, w2a.z, w2a.w, w2b.x, w2b.y, w2b.z, w2b.w};
;         float um2[8], um1[8], u0[8], u1[8], b0[8], b1[8];
;         unpack8(um2v, um2); unpack8(um1v, um1); unpack8(u0v, u0); unpack8(u1v, u1);
; #pragma unroll
;         for (int j = 0; j < 8; ++j) { um2[j] = halo ? um2[j] : 0.f; um1[j] = halo ? um1[j] : 0.f; }
;         unpack8(b0v, b0); unpack8(b1v, b1);
;         float y0[8], y1[8];
; #pragma unroll
;         for (int j = 0; j < 8; ++j) { y0[j] = b0[j] * (w2[j] * u0[j] + w0[j] * um2[j] + w1[j] * um1[j]); y1[j] = b1[j] * (w2[j] * u1[j] + w0[j] * um1[j] + w1[j] * u0[j]); ss0 += y0[j] * y0[j]; ss1 += y1[j] * y1[j]; }
;         *(LAS u32x4*)(scr + c0 * 2) = pack8(y0); *(LAS u32x4*)(scr + 8192 + c0 * 2) = pack8(y1);
	v_pk_mul_f32 v[116:117], v[72:73], v[124:125] op_sel_hi:[0,1]
	v_pk_mul_f32 v[50:51], v[72:73], v[50:51] op_sel:[1,0]
	v_pk_mul_f32 v[72:73], v[74:75], v[126:127] op_sel_hi:[0,1]
	v_mov_b32_e32 v74, v75
	v_cndmask_b32_e64 v110, v98, 0, s[0:1]
	v_cndmask_b32_e64 v45, v45, 0, s[0:1]
	v_cndmask_b32_e64 v111, v107, 0, s[0:1]
	v_cndmask_b32_e64 v113, v113, 0, s[0:1]
	v_lshlrev_b32_e32 v98, 16, v58
	v_and_b32_e32 v100, 0xffff0000, v58
	v_lshlrev_b32_e32 v102, 16, v59
	v_and_b32_e32 v4, 0xffff0000, v59
	v_pk_mov_b32 v[58:59], v[46:47], v[124:125] op_sel:[1,0]
	v_pk_fma_f32 v[36:37], v[42:43], v[36:37], v[120:121] op_sel_hi:[1,0,1]
	v_pk_fma_f32 v[42:43], v[118:119], v[60:61], v[48:49] op_sel:[0,1,0]
	v_pk_fma_f32 v[38:39], v[40:41], v[38:39], v[68:69] op_sel_hi:[1,0,1]
	v_pk_mul_f32 v[40:41], v[70:71], v[114:115] op_sel_hi:[0,1]
	v_pk_fma_f32 v[46:47], v[46:47], v[32:33], v[116:117] op_sel_hi:[1,0,1]
	v_pk_fma_f32 v[32:33], v[108:109], v[32:33], v[50:51] op_sel:[0,1,0]
	v_pk_mul_f32 v[48:49], v[74:75], v[128:129] op_sel_hi:[0,1]
	v_lshlrev_b32_e32 v92, 16, v56
	v_and_b32_e32 v94, 0xffff0000, v56
	v_lshlrev_b32_e32 v96, 16, v57
	v_and_b32_e32 v2, 0xffff0000, v57
	v_pk_mov_b32 v[56:57], v[44:45], v[114:115] op_sel:[1,0]
	v_pk_mov_b32 v[132:133], v[110:111], v[126:127] op_sel:[1,0]
	v_pk_mov_b32 v[134:135], v[112:113], v[128:129] op_sel:[1,0]
	v_mov_b32_e32 v136, v63
	v_mov_b32_e32 v138, v67
	v_pk_fma_f32 v[34:35], v[110:111], v[34:35], v[72:73] op_sel_hi:[1,0,1]
	v_pk_fma_f32 v[36:37], v[60:61], v[52:53], v[36:37] op_sel_hi:[0,1,1]
	v_pk_fma_f32 v[38:39], v[54:55], v[62:63], v[38:39] op_sel_hi:[1,0,1]
	v_pk_fma_f32 v[40:41], v[44:45], v[104:105], v[40:41] op_sel_hi:[1,0,1]
	v_pk_fma_f32 v[44:45], v[58:59], v[64:65], v[46:47] op_sel_hi:[1,0,1]
	v_pk_fma_f32 v[32:33], v[130:131], v[64:65], v[32:33] op_sel:[0,1,0]
	v_pk_fma_f32 v[46:47], v[112:113], v[106:107], v[48:49] op_sel_hi:[1,0,1]
	v_pk_fma_f32 v[34:35], v[132:133], v[66:67], v[34:35] op_sel_hi:[1,0,1]
	v_pk_mul_f32 v[36:37], v[36:37], v[92:93]
	v_pk_mul_f32 v[92:93], v[38:39], v[96:97]
	v_pk_fma_f32 v[38:39], v[56:57], v[136:137], v[40:41] op_sel_hi:[1,0,1]
	v_pk_mul_f32 v[96:97], v[32:33], v[100:101]
	v_pk_fma_f32 v[32:33], v[134:135], v[138:139], v[46:47] op_sel_hi:[1,0,1]
	v_pk_mul_f32 v[42:43], v[42:43], v[94:95]
	v_pk_mul_f32 v[94:95], v[44:45], v[98:99]
	v_pk_mul_f32 v[98:99], v[34:35], v[102:103]
	v_pk_fma_f32 v[8:9], v[36:37], v[36:37], v[8:9]
	v_pk_mul_f32 v[100:101], v[38:39], v[2:3]
	v_pk_mul_f32 v[102:103], v[32:33], v[4:5]
	v_cvt_pk_bf16_f32 v2, v36, v42
	v_cvt_pk_bf16_f32 v3, v92, v100
	v_cvt_pk_bf16_f32 v4, v94, v96
	v_pk_fma_f32 v[8:9], v[42:43], v[42:43], v[8:9]
	v_cvt_pk_bf16_f32 v5, v98, v102
	ds_write_b128 v31, v[2:5]
	v_cvt_pk_bf16_f32 v2, v37, v43
	v_cvt_pk_bf16_f32 v3, v93, v101
	v_cvt_pk_bf16_f32 v4, v95, v97
	v_cvt_pk_bf16_f32 v5, v99, v103
	v_pk_fma_f32 v[8:9], v[92:93], v[92:93], v[8:9]
	ds_write_b128 v31, v[2:5] offset:8192
	v_pk_fma_f32 v[8:9], v[100:101], v[100:101], v[8:9]
	v_lshl_add_u64 v[6:7], v[6:7], 0, s[28:29]
	v_pk_fma_f32 v[2:3], v[94:95], v[94:95], v[8:9]
	s_waitcnt vmcnt(11)
	v_and_b32_e32 v83, 0xffff0000, v184
	v_pk_fma_f32 v[2:3], v[96:97], v[96:97], v[2:3]
	s_waitcnt vmcnt(10)
	v_and_b32_e32 v89, 0xffff0000, v188
	v_pk_fma_f32 v[2:3], v[98:99], v[98:99], v[2:3]
	s_waitcnt vmcnt(8)
	v_lshlrev_b32_e32 v79, 16, v196
	v_lshlrev_b32_e32 v78, 16, v192
	v_lshlrev_b32_e32 v96, 16, v184
	v_lshlrev_b32_e32 v97, 16, v188
	v_pk_fma_f32 v[2:3], v[102:103], v[102:103], v[2:3]
	v_lshlrev_b32_e32 v102, 16, v190
	v_and_b32_e32 v104, 0xffff0000, v190
	v_and_b32_e32 v106, 0xffff0000, v186
	v_lshlrev_b32_e32 v108, 16, v187
	v_lshlrev_b32_e32 v107, 16, v191
	v_and_b32_e32 v109, 0xffff0000, v191
	v_lshlrev_b32_e32 v191, 16, v199
	v_lshlrev_b32_e32 v190, 16, v195
	v_cndmask_b32_e64 v83, v83, 0, s[0:1]
	v_cndmask_b32_e64 v92, v89, 0, s[0:1]
	v_cndmask_b32_e64 v97, v97, 0, s[0:1]
	v_cndmask_b32_e64 v96, v96, 0, s[0:1]
	s_waitcnt vmcnt(5)
	v_pk_mul_f32 v[98:99], v[208:209], v[78:79] op_sel_hi:[0,1]
	v_lshlrev_b32_e32 v85, 16, v185
	v_lshlrev_b32_e32 v91, 16, v189
	v_and_b32_e32 v93, 0xffff0000, v189
	v_and_b32_e32 v100, 0xffff0000, v185
	v_lshlrev_b32_e32 v9, 16, v197
	v_lshlrev_b32_e32 v8, 16, v193
	v_and_b32_e32 v185, 0xffff0000, v196
	v_and_b32_e32 v184, 0xffff0000, v192
	s_waitcnt vmcnt(2)
	v_mov_b32_e32 v86, v223
	v_cndmask_b32_e64 v105, v104, 0, s[0:1]
	v_cndmask_b32_e64 v104, v106, 0, s[0:1]
	v_cndmask_b32_e64 v107, v107, 0, s[0:1]
	v_cndmask_b32_e64 v106, v108, 0, s[0:1]
	v_pk_mul_f32 v[222:223], v[222:223], v[190:191] op_sel_hi:[0,1]
	v_pk_fma_f32 v[98:99], v[96:97], v[212:213], v[98:99] op_sel_hi:[1,0,1]
	v_pk_mov_b32 v[78:79], v[96:97], v[78:79] op_sel:[1,0]
	v_mul_f32_e32 v212, v83, v213
	v_mul_f32_e32 v213, v92, v213
	v_lshlrev_b32_e32 v87, 16, v186
	v_and_b32_e32 v4, 0xffff0000, v193
	v_and_b32_e32 v5, 0xffff0000, v197
	v_lshlrev_b32_e32 v76, 16, v200
	v_lshlrev_b32_e32 v77, 16, v204
	v_lshlrev_b32_e32 v186, 16, v194
	v_and_b32_e32 v188, 0xffff0000, v194
	v_and_b32_e32 v192, 0xffff0000, v195
	v_and_b32_e32 v195, 0xffff0000, v204
	v_and_b32_e32 v194, 0xffff0000, v200
	v_lshlrev_b32_e32 v200, 16, v202
	v_and_b32_e32 v204, 0xffff0000, v202
	v_mov_b32_e32 v202, v211
	s_waitcnt vmcnt(1)
; #define LAS __attribute__((address_space(3)))
; __device__ __forceinline__ void unpack8(const u32x4 v, float (&f)[8]) { f[0] = bflo(v.x); f[1] = bfhi(v.x); f[2] = bflo(v.y); f[3] = bfhi(v.y); f[4] = bflo(v.z); f[5] = bfhi(v.z); f[6] = bflo(v.w); f[7] = bfhi(v.w); }
; __device__ __forceinline__ u32x4 pack8(const float (&f)[8]) { u32x4 o; o.x = cvtpk(f[0], f[1]); o.y = cvtpk(f[2], f[3]); o.z = cvtpk(f[4], f[5]); o.w = cvtpk(f[6], f[7]); return o; }
; __device__ __forceinline__ void p3_rows2(int row0, const bf16* PROJ, const float* sc_w, const float* sc_nw, const float* ssd_nw, const float* SSQ, bf16* Y, LAS unsigned char* scr, int lane) {
;     ...
;         unpack8(um2v, um2); unpack8(um1v, um1); unpack8(u0v, u0); unpack8(u1v, u1);
; #pragma unroll
;         for (int j = 0; j < 8; ++j) { um2[j] = halo ? um2[j] : 0.f; um1[j] = halo ? um1[j] : 0.f; }
;         unpack8(b0v, b0); unpack8(b1v, b1);
;         float y0[8], y1[8];
; #pragma unroll
;         for (int j = 0; j < 8; ++j) { y0[j] = b0[j] * (w2[j] * u0[j] + w0[j] * um2[j] + w1[j] * um1[j]); y1[j] = b1[j] * (w2[j] * u1[j] + w0[j] * um1[j] + w1[j] * u0[j]); ss0 += y0[j] * y0[j]; ss1 += y1[j] * y1[j]; }
;         *(LAS u32x4*)(scr + c0 * 2) = pack8(y0); *(LAS u32x4*)(scr + 8192 + c0 * 2) = pack8(y1);
	v_mov_b32_e32 v88, v143
	v_cndmask_b32_e64 v94, v85, 0, s[0:1]
	v_cndmask_b32_e64 v95, v91, 0, s[0:1]
	v_cndmask_b32_e64 v101, v93, 0, s[0:1]
	v_mov_b32_e32 v93, v184
	v_pk_mul_f32 v[210:211], v[210:211], v[8:9] op_sel_hi:[0,1]
	v_pk_fma_f32 v[142:143], v[106:107], v[142:143], v[222:223] op_sel_hi:[1,0,1]
	v_pk_mov_b32 v[190:191], v[106:107], v[190:191] op_sel:[1,0]
	v_pk_fma_f32 v[222:223], v[216:217], v[78:79], v[98:99] op_sel_hi:[0,1,1]
	v_pk_fma_f32 v[184:185], v[208:209], v[184:185], v[212:213] op_sel:[1,0,0]
	v_and_b32_e32 v110, 0xffff0000, v187
	v_lshlrev_b32_e32 v187, 16, v198
	v_and_b32_e32 v189, 0xffff0000, v198
	v_and_b32_e32 v193, 0xffff0000, v199
	v_lshlrev_b32_e32 v196, 16, v201
	v_lshlrev_b32_e32 v197, 16, v205
	v_and_b32_e32 v199, 0xffff0000, v205
	v_and_b32_e32 v198, 0xffff0000, v201
	v_lshlrev_b32_e32 v201, 16, v206
	v_and_b32_e32 v205, 0xffff0000, v206
	v_lshlrev_b32_e32 v80, 16, v203
	v_and_b32_e32 v206, 0xffff0000, v203
	v_mov_b32_e32 v82, v215
	v_cndmask_b32_e64 v100, v100, 0, s[0:1]
	v_pk_mul_f32 v[202:203], v[202:203], v[4:5] op_sel_hi:[0,1]
	v_pk_fma_f32 v[210:211], v[94:95], v[214:215], v[210:211] op_sel_hi:[1,0,1]
	v_pk_mov_b32 v[8:9], v[94:95], v[8:9] op_sel:[1,0]
	s_waitcnt vmcnt(0)
	v_pk_fma_f32 v[142:143], v[190:191], v[226:227], v[142:143] op_sel_hi:[1,0,1]
	v_pk_mul_f32 v[190:191], v[222:223], v[76:77]
	v_pk_fma_f32 v[184:185], v[92:93], v[216:217], v[184:185] op_sel:[0,1,0]
	v_mov_b32_e32 v84, v219
	v_cndmask_b32_e64 v103, v102, 0, s[0:1]
	v_cndmask_b32_e64 v102, v87, 0, s[0:1]
	v_cndmask_b32_e64 v109, v109, 0, s[0:1]
	v_cndmask_b32_e64 v108, v110, 0, s[0:1]
	v_pk_mul_f32 v[110:111], v[220:221], v[186:187] op_sel_hi:[0,1]
	v_pk_mul_f32 v[220:221], v[220:221], v[188:189] op_sel:[1,0]
	v_pk_mul_f32 v[86:87], v[86:87], v[192:193] op_sel_hi:[0,1]
	v_pk_fma_f32 v[202:203], v[100:101], v[82:83], v[202:203] op_sel_hi:[1,0,1]
	v_pk_mov_b32 v[4:5], v[100:101], v[4:5] op_sel:[1,0]
	v_pk_fma_f32 v[8:9], v[8:9], v[218:219], v[210:211] op_sel_hi:[1,0,1]
	v_pk_fma_f32 v[2:3], v[190:191], v[190:191], v[2:3]
	v_pk_mul_f32 v[184:185], v[184:185], v[194:195]
	v_mov_b32_e32 v90, v227
	v_pk_fma_f32 v[214:215], v[102:103], v[140:141], v[110:111] op_sel_hi:[1,0,1]
	v_pk_mov_b32 v[186:187], v[102:103], v[186:187] op_sel:[1,0]
	v_pk_fma_f32 v[140:141], v[104:105], v[140:141], v[220:221] op_sel:[0,1,0]
	v_pk_mov_b32 v[188:189], v[104:105], v[188:189] op_sel:[1,0]
	v_pk_fma_f32 v[220:221], v[108:109], v[88:89], v[86:87] op_sel_hi:[1,0,1]
	v_pk_mov_b32 v[192:193], v[108:109], v[192:193] op_sel:[1,0]
	v_pk_fma_f32 v[4:5], v[4:5], v[84:85], v[202:203] op_sel_hi:[1,0,1]
	v_pk_mul_f32 v[8:9], v[8:9], v[196:197]
	v_pk_fma_f32 v[194:195], v[184:185], v[184:185], v[2:3]
	v_lshlrev_b32_e32 v81, 16, v207
	v_and_b32_e32 v207, 0xffff0000, v207
	v_pk_fma_f32 v[186:187], v[186:187], v[224:225], v[214:215] op_sel_hi:[1,0,1]
	v_pk_fma_f32 v[140:141], v[188:189], v[224:225], v[140:141] op_sel:[0,1,0]
	v_pk_fma_f32 v[188:189], v[192:193], v[90:91], v[220:221] op_sel_hi:[1,0,1]
	v_pk_mul_f32 v[192:193], v[4:5], v[198:199]
	v_cvt_pk_bf16_f32 v2, v190, v184
	v_pk_fma_f32 v[194:195], v[8:9], v[8:9], v[194:195]
	v_cvt_pk_bf16_f32 v3, v8, v192
	v_pk_mul_f32 v[186:187], v[186:187], v[200:201]
	v_pk_mul_f32 v[140:141], v[140:141], v[204:205]
	v_pk_mul_f32 v[142:143], v[142:143], v[80:81]
	v_pk_mul_f32 v[188:189], v[188:189], v[206:207]
	v_cvt_pk_bf16_f32 v4, v186, v140
	s_nop 0
	v_cvt_pk_bf16_f32 v5, v142, v188
	ds_write_b128 v31, v[2:5] offset:1024
	v_cvt_pk_bf16_f32 v2, v191, v185
	v_cvt_pk_bf16_f32 v3, v9, v193
	v_pk_fma_f32 v[8:9], v[192:193], v[192:193], v[194:195]
	v_cvt_pk_bf16_f32 v4, v187, v141
	v_cvt_pk_bf16_f32 v5, v143, v189
	ds_write_b128 v31, v[2:5] offset:9216
	v_pk_fma_f32 v[2:3], v[186:187], v[186:187], v[8:9]
	v_add_u32_e32 v31, 0x800, v31
	v_pk_fma_f32 v[2:3], v[140:141], v[140:141], v[2:3]
	s_nop 0
	v_pk_fma_f32 v[2:3], v[142:143], v[142:143], v[2:3]
	s_nop 0
	v_pk_fma_f32 v[8:9], v[188:189], v[188:189], v[2:3]
	s_cbranch_scc0 .LBB0_485
; __device__ __forceinline__ float wave_sum(float v) {
; #pragma unroll
;     for (int o = 1; o < 64; o <<= 1) v += __shfl_xor(v, o);
;     return v;
; }
; __device__ __forceinline__ void p3_rows2(int row0, const bf16* PROJ, const float* sc_w, const float* sc_nw, const float* ssd_nw, const float* SSQ, bf16* Y, LAS unsigned char* scr, int lane) {
;     ...
;     const float rs0 = 1.0f / sqrtf(wave_sum(ss0) * (1.f / D_CONV) + EPS), rs1 = 1.0f / sqrtf(wave_sum(ss1) * (1.f / D_CONV) + EPS);
	v_and_b32_e32 v4, 64, v30
	v_add_u32_e32 v2, 64, v4
	v_xor_b32_e32 v3, 1, v30
	v_cmp_lt_i32_e32 vcc, v3, v2
	v_xor_b32_e32 v6, 2, v30
	v_xor_b32_e32 v24, 8, v30
	v_cndmask_b32_e32 v3, v30, v3, vcc
	v_lshlrev_b32_e32 v5, 2, v3
	ds_bpermute_b32 v3, v5, v8
	v_cmp_lt_i32_e32 vcc, v6, v2
	v_xor_b32_e32 v25, 16, v30
	v_xor_b32_e32 v26, 32, v30
	v_cndmask_b32_e32 v6, v30, v6, vcc
	s_waitcnt lgkmcnt(0)
	v_add_f32_e32 v3, v8, v3
	v_lshlrev_b32_e32 v6, 2, v6
	ds_bpermute_b32 v7, v6, v3
	v_xor_b32_e32 v8, 4, v30
	v_cmp_lt_i32_e32 vcc, v8, v2
	s_waitcnt lgkmcnt(0)
	v_add_f32_e32 v3, v3, v7
	v_cndmask_b32_e32 v7, v30, v8, vcc
	v_lshlrev_b32_e32 v7, 2, v7
	ds_bpermute_b32 v8, v7, v3
	v_cmp_lt_i32_e32 vcc, v24, v2
	s_waitcnt lgkmcnt(0)
	v_add_f32_e32 v3, v3, v8
	v_cndmask_b32_e32 v8, v30, v24, vcc
	v_lshlrev_b32_e32 v8, 2, v8
	ds_bpermute_b32 v24, v8, v3
	v_cmp_lt_i32_e32 vcc, v25, v2
	s_waitcnt lgkmcnt(0)
	v_add_f32_e32 v3, v3, v24
	v_cndmask_b32_e32 v24, v30, v25, vcc
	v_cmp_lt_i32_e32 vcc, v26, v2
	v_lshlrev_b32_e32 v24, 2, v24
	ds_bpermute_b32 v25, v24, v3
	v_cndmask_b32_e32 v2, v30, v26, vcc
	ds_bpermute_b32 v26, v5, v9
	v_lshlrev_b32_e32 v2, 2, v2
	s_waitcnt lgkmcnt(1)
	v_add_f32_e32 v3, v3, v25
	ds_bpermute_b32 v25, v2, v3
	s_waitcnt lgkmcnt(1)
	v_add_f32_e32 v9, v9, v26
	ds_bpermute_b32 v26, v6, v9
	s_waitcnt lgkmcnt(1)
	v_add_f32_e32 v3, v3, v25
	v_fmamk_f32 v3, v3, 0x39800000, v28
	s_waitcnt lgkmcnt(0)
	v_add_f32_e32 v9, v9, v26
	ds_bpermute_b32 v26, v7, v9
	v_mul_f32_e32 v25, 0x4f800000, v3
	v_cmp_gt_f32_e32 vcc, s36, v3
	s_waitcnt lgkmcnt(0)
	v_add_f32_e32 v9, v9, v26
	ds_bpermute_b32 v8, v8, v9
	v_cndmask_b32_e32 v3, v3, v25, vcc
	v_sqrt_f32_e32 v25, v3
	s_waitcnt lgkmcnt(0)
	v_add_f32_e32 v8, v9, v8
	v_add_u32_e32 v27, -1, v25
	ds_bpermute_b32 v9, v24, v8
	v_fma_f32 v31, -v27, v25, v3
	v_cmp_ge_f32_e64 s[0:1], 0, v31
	v_add_u32_e32 v31, 1, v25
	s_waitcnt lgkmcnt(0)
	v_add_f32_e32 v8, v8, v9
	v_cndmask_b32_e64 v27, v25, v27, s[0:1]
	v_fma_f32 v25, -v31, v25, v3
	v_cmp_lt_f32_e64 s[0:1], 0, v25
	ds_bpermute_b32 v2, v2, v8
	s_waitcnt lgkmcnt(0)
	v_add_f32_e32 v2, v8, v2
	v_cndmask_b32_e64 v25, v27, v31, s[0:1]
	v_mul_f32_e32 v27, 0x37800000, v25
	v_cndmask_b32_e32 v25, v25, v27, vcc
	v_cmp_class_f32_e32 vcc, v3, v29
	v_fmamk_f32 v2, v2, 0x39800000, v28
	v_mul_f32_e32 v8, 0x4f800000, v2
	v_cndmask_b32_e32 v3, v25, v3, vcc
	v_div_scale_f32 v26, s[0:1], v3, v3, 1.0
	v_rcp_f32_e32 v27, v26
	s_lshl_b64 s[0:1], s[16:17], 14
	v_lshl_add_u64 v[24:25], v[16:17], 0, s[0:1]
	v_cmp_gt_f32_e64 s[0:1], s36, v2
	v_fma_f32 v31, -v26, v27, 1.0
	v_fmac_f32_e32 v27, v31, v27
	v_cndmask_b32_e64 v2, v2, v8, s[0:1]
	v_div_scale_f32 v9, vcc, 1.0, v3, 1.0
	v_sqrt_f32_e32 v8, v2
	v_mul_f32_e32 v31, v9, v27
	v_fma_f32 v32, -v26, v31, v9
	v_fmac_f32_e32 v31, v32, v27
	v_fma_f32 v9, -v26, v31, v9
	v_add_u32_e32 v26, -1, v8
	v_fma_f32 v32, -v26, v8, v2
	v_cmp_ge_f32_e64 s[4:5], 0, v32
	v_add_u32_e32 v32, 1, v8
	s_nop 0
	v_cndmask_b32_e64 v26, v8, v26, s[4:5]
	v_fma_f32 v8, -v32, v8, v2
	v_cmp_lt_f32_e64 s[4:5], 0, v8
	s_nop 1
	v_cndmask_b32_e64 v8, v26, v32, s[4:5]
	v_mul_f32_e32 v26, 0x37800000, v8
	v_cndmask_b32_e64 v8, v8, v26, s[0:1]
	v_cmp_class_f32_e64 s[0:1], v2, v29
	s_nop 1
	v_cndmask_b32_e64 v2, v8, v2, s[0:1]
	v_div_scale_f32 v26, s[0:1], v2, v2, 1.0
	v_rcp_f32_e32 v32, v26
	v_div_fmas_f32 v8, v9, v27, v31
	v_div_fixup_f32 v8, v8, v3, 1.0
	s_mov_b64 s[0:1], 0
	v_fma_f32 v3, -v26, v32, 1.0
	v_fmac_f32_e32 v32, v3, v32
	v_div_scale_f32 v3, vcc, 1.0, v2, 1.0
	v_mul_f32_e32 v9, v3, v32
	v_fma_f32 v27, -v26, v9, v3
	v_fmac_f32_e32 v9, v27, v32
	v_fma_f32 v3, -v26, v9, v3
	v_div_fmas_f32 v3, v3, v32, v9
	v_div_fixup_f32 v9, v3, v2, 1.0
	v_mov_b64_e32 v[2:3], v[20:21]
	v_mov_b32_e32 v26, v1
